# dilated attention tile loop: in-place PV accumulators (no per-tile copy moves), batched K/V/bias LDS reads with counted lgkmcnt
# speedup vs baseline: 1.0249x; 1.0123x over previous
.LBB0_1688:
	v_sub_f32_e32 v36, v52, v158
	v_sub_f32_e32 v2, v2, v158
	v_exp_f32_e32 v36, v36
	v_exp_f32_e32 v2, v2
	v_cndmask_b32_e64 v38, v36, 0, s[4:5]
	v_add_f32_e32 v37, v36, v2
	v_cndmask_b32_e64 v36, 0, v36, s[4:5]
	v_cvt_pk_bf16_f32 v36, v36, v38
	v_cndmask_b32_e64 v38, v2, 0, s[4:5]
	v_cndmask_b32_e64 v2, 0, v2, s[4:5]
	v_cvt_pk_bf16_f32 v2, v2, v38
	v_cndmask_b32_e64 v84, 0, v36, s[14:15]
	v_cndmask_b32_e64 v88, 0, v2, s[14:15]
	v_cndmask_b32_e64 v85, 0, v36, s[16:17]
	v_cndmask_b32_e64 v89, 0, v2, s[16:17]
	v_cndmask_b32_e64 v86, 0, v36, s[18:19]
	v_cndmask_b32_e64 v90, 0, v2, s[18:19]
	v_cndmask_b32_e64 v87, 0, v36, s[20:21]
	v_cndmask_b32_e64 v91, 0, v2, s[20:21]
	v_add_f32_e32 v130, v157, v37
	v_mov_b32_e32 v2, v158
.LBB0_1689:
	s_setprio 1
	s_waitcnt lgkmcnt(0)
	v_mfma_f32_32x32x16_bf16 v[20:35], v[186:189], v[84:87], v[20:35]
	v_mfma_f32_32x32x16_bf16 v[4:19], v[190:193], v[84:87], v[4:19]
	v_mfma_f32_32x32x16_bf16 v[20:35], v[194:197], v[88:91], v[20:35]
	v_mfma_f32_32x32x16_bf16 v[4:19], v[198:201], v[88:91], v[4:19]
	s_setprio 0
	v_mov_b32_e32 v158, v2
	v_mov_b32_e32 v157, v130

.LBB0_1709:
	s_or_b64 exec, exec, s[34:35]
	v_cmp_le_u32_e32 vcc, s49, v144
	s_and_saveexec_b64 s[34:35], vcc
	s_cbranch_execz .LBB0_1690
	s_lshl_b32 s36, s46, 14
	s_add_i32 s38, s36, 0
	s_setprio 1
	v_add3_u32 v2, s38, v140, v139
	v_add3_u32 v202, s38, v141, v139
	v_add3_u32 v203, s38, v142, v139
	v_add3_u32 v204, s38, v143, v139
	ds_read_b128 v[36:39], v2 offset:16640
	ds_read_b128 v[52:55], v202 offset:16640
	ds_read_b128 v[178:181], v203 offset:16640
	ds_read_b128 v[182:185], v204 offset:16640
	v_add3_u32 v202, s38, v145, v152
	v_add3_u32 v203, s38, v146, v152
	ds_read_b128 v[186:189], v202 offset:24832
	ds_read_b128 v[190:193], v202 offset:26880
	ds_read_b128 v[194:197], v203 offset:24832
	ds_read_b128 v[198:201], v203 offset:26880
	s_waitcnt lgkmcnt(7)
	v_mfma_f32_32x32x16_bf16 v[36:51], v[36:39], v[92:95], 0
	s_waitcnt lgkmcnt(6)
	v_mfma_f32_32x32x16_bf16 v[36:51], v[52:55], v[96:99], v[36:51]
	s_waitcnt lgkmcnt(5)
	v_mfma_f32_32x32x16_bf16 v[36:51], v[178:181], v[100:103], v[36:51]
	s_waitcnt lgkmcnt(4)
	v_mfma_f32_32x32x16_bf16 v[36:51], v[182:185], v[104:107], v[36:51]
	s_setprio 0
	s_mov_b64 s[36:37], -1
	s_cmp_ge_i32 s47, s42
	v_add_f32_e32 v159, 0x41000000, v158
	s_cbranch_scc0 .LBB0_1714
	v_add_u32_e32 v2, 0x1e7c, v156
	v_add_u32_e32 v205, 0x1e74, v156
	v_add_u32_e32 v56, 0x1e5c, v156
	v_add_u32_e32 v58, 0x1e54, v156
	ds_read2_b32 v[52:53], v2 offset1:1
	ds_read2_b32 v[54:55], v205 offset1:1
	ds_read2_b32 v[56:57], v56 offset1:1
	ds_read2_b32 v[58:59], v58 offset1:1
	v_add_u32_e32 v2, 0x1e3c, v156
	v_add_u32_e32 v205, 0x1e34, v156
	v_add_u32_e32 v235, 0x1e1c, v156
	v_add_u32_e32 v236, 0x1e14, v156
	ds_read2_b32 v[206:207], v2 offset1:1
	ds_read2_b32 v[208:209], v205 offset1:1
	ds_read2_b32 v[210:211], v235 offset1:1
	ds_read2_b32 v[212:213], v236 offset1:1
	s_waitcnt lgkmcnt(4)
	v_pk_fma_f32 v[130:131], v[36:37], s[82:83], v[52:53] op_sel:[0,0,1] op_sel_hi:[1,0,0]
	v_pk_fma_f32 v[88:89], v[38:39], s[82:83], v[54:55] op_sel:[0,0,1] op_sel_hi:[1,0,0]
	v_max_f32_e32 v2, v130, v131
	v_max_f32_e32 v52, v88, v89
	v_pk_fma_f32 v[86:87], v[40:41], s[82:83], v[56:57] op_sel:[0,0,1] op_sel_hi:[1,0,0]
	v_pk_fma_f32 v[84:85], v[42:43], s[82:83], v[58:59] op_sel:[0,0,1] op_sel_hi:[1,0,0]
	v_max3_f32 v2, v2, s90, v52
	v_max_f32_e32 v52, v86, v87
	v_max_f32_e32 v53, v84, v85
	v_max3_f32 v2, v2, v52, v53
	s_waitcnt lgkmcnt(0)
	v_pk_fma_f32 v[136:137], v[44:45], s[82:83], v[206:207] op_sel:[0,0,1] op_sel_hi:[1,0,0]
	v_mov_b32_e32 v160, v157
	v_pk_fma_f32 v[134:135], v[46:47], s[82:83], v[208:209] op_sel:[0,0,1] op_sel_hi:[1,0,0]
	v_max_f32_e32 v52, v136, v137
	v_max_f32_e32 v53, v134, v135
	v_pk_fma_f32 v[132:133], v[48:49], s[82:83], v[210:211] op_sel:[0,0,1] op_sel_hi:[1,0,0]
	v_pk_fma_f32 v[90:91], v[50:51], s[82:83], v[212:213] op_sel:[0,0,1] op_sel_hi:[1,0,0]
	v_max3_f32 v2, v2, v52, v53
	v_max_f32_e32 v52, v132, v133
	v_max_f32_e32 v53, v90, v91
	v_max3_f32 v2, v2, v52, v53
	v_and_b32_e32 v53, 64, v214
	v_xor_b32_e32 v52, 32, v214
	v_add_u32_e32 v53, 64, v53
	v_cmp_lt_i32_e32 vcc, v52, v53
	s_nop 1
	v_cndmask_b32_e32 v52, v214, v52, vcc
	v_lshlrev_b32_e32 v52, 2, v52
	ds_bpermute_b32 v52, v52, v2
	s_waitcnt lgkmcnt(0)
	v_max_f32_e32 v52, v52, v52
	v_max_f32_e32 v161, v2, v52
	v_cmp_gt_f32_e32 vcc, v161, v159
	v_mov_b32_e32 v2, v158
	s_cbranch_vccz .LBB0_1713
	v_max_f32_e32 v2, v161, v161
	v_max_f32_e32 v52, v158, v158
	v_max_f32_e32 v2, v52, v2
	v_sub_f32_e32 v52, v158, v2
	v_exp_f32_e32 v160, v52
	s_nop 0
	v_pk_mul_f32 v[34:35], v[34:35], v[160:161] op_sel_hi:[1,0]
	v_pk_mul_f32 v[32:33], v[32:33], v[160:161] op_sel_hi:[1,0]
	v_pk_mul_f32 v[30:31], v[30:31], v[160:161] op_sel_hi:[1,0]
	v_pk_mul_f32 v[28:29], v[28:29], v[160:161] op_sel_hi:[1,0]
	v_pk_mul_f32 v[26:27], v[26:27], v[160:161] op_sel_hi:[1,0]
	v_pk_mul_f32 v[24:25], v[24:25], v[160:161] op_sel_hi:[1,0]
	v_pk_mul_f32 v[22:23], v[22:23], v[160:161] op_sel_hi:[1,0]
	v_pk_mul_f32 v[20:21], v[20:21], v[160:161] op_sel_hi:[1,0]
	v_pk_mul_f32 v[18:19], v[18:19], v[160:161] op_sel_hi:[1,0]
	v_pk_mul_f32 v[16:17], v[16:17], v[160:161] op_sel_hi:[1,0]
	v_pk_mul_f32 v[14:15], v[14:15], v[160:161] op_sel_hi:[1,0]
	v_pk_mul_f32 v[12:13], v[12:13], v[160:161] op_sel_hi:[1,0]
	v_pk_mul_f32 v[10:11], v[10:11], v[160:161] op_sel_hi:[1,0]
	v_pk_mul_f32 v[8:9], v[8:9], v[160:161] op_sel_hi:[1,0]
	v_pk_mul_f32 v[6:7], v[6:7], v[160:161] op_sel_hi:[1,0]
	v_pk_mul_f32 v[4:5], v[4:5], v[160:161] op_sel_hi:[1,0]
	v_mul_f32_e32 v160, v157, v160
